# stack: P9 epilogue rope prefetch + E2 unit order with bid bit7 flipped (balance 9th round) + lg_barrier buffer_inv issued right after arrive atomic
# baseline (speedup 1.0000x reference)
; __device__ __forceinline__ unsigned xb_ld(unsigned* p)              { return __hip_atomic_load(p, __ATOMIC_RELAXED, __HIP_MEMORY_SCOPE_AGENT); }
; __device__ __forceinline__ unsigned xb_add(unsigned* p, unsigned v) { return __hip_atomic_fetch_add(p, v, __ATOMIC_RELAXED, __HIP_MEMORY_SCOPE_AGENT); }
; #define XB_SPIN(cond, bar) do { unsigned _sp = 0; while (cond) { __builtin_amdgcn_s_sleep(1); \
;     if ((++_sp & 255u) == 0u) { if (xb_ld(&(bar)[XB_TMO])) break; if (_sp > XB_SPIN_CAP) { atomicAdd(&(bar)[XB_TMO], 1u); break; } } } } while (0)
; __device__ __forceinline__ void lg_barrier(const XcdBarrier& b, int wave, unsigned g, unsigned nloc, bool fast) {
;     ...
;         const unsigned old = xb_add(&bar[LG_SUB(g)], 1u), gen = old / nloc;
;         if (old + 1u == (gen + 1u) * nloc) xb_add(&bar[LG_GEN(g)], 1u);
;         else XB_SPIN(xb_ld(&bar[LG_GEN(g)]) == gen, bar);
;         __builtin_amdgcn_fence(__ATOMIC_ACQUIRE, "agent");
;         asm volatile("s_waitcnt vmcnt(0)" ::: "memory");
.LBB0_817:
	s_or_b64 exec, exec, s[10:11]
	buffer_inv sc1
	s_waitcnt vmcnt(0)
	v_readfirstlane_b32 s8, v1
	s_mov_b64 s[10:11], -1
	s_nop 0
	v_add_u32_e32 v2, s8, v0
	s_add_u32 s8, s6, 0x4100
	v_and_b32_e32 v0, 31, v2
	s_addc_u32 s9, s7, 0
	v_cmp_ne_u32_e32 vcc, 31, v0
	v_mov_b64_e32 v[0:1], s[8:9]
	s_and_saveexec_b64 s[6:7], vcc
	s_cbranch_execz .LBB0_829
	v_mov_b32_e32 v0, 0
	global_load_dword v3, v0, s[8:9] sc1
	v_lshrrev_b32_e32 v1, 5, v2
	s_mov_b64 s[14:15], 0
	s_waitcnt vmcnt(0)
	v_cmp_eq_u32_e32 vcc, v3, v1
	s_and_saveexec_b64 s[12:13], vcc
	s_cbranch_execz .LBB0_828
	s_add_u32 s10, s80, 0x4200
	s_addc_u32 s11, s81, 0
	s_mov_b32 s24, 1
	s_branch .LBB0_821

; __device__ __forceinline__ unsigned xb_ld(unsigned* p)              { return __hip_atomic_load(p, __ATOMIC_RELAXED, __HIP_MEMORY_SCOPE_AGENT); }
; #define XB_SPIN(cond, bar) do { unsigned _sp = 0; while (cond) { __builtin_amdgcn_s_sleep(1); \
;     if ((++_sp & 255u) == 0u) { if (xb_ld(&(bar)[XB_TMO])) break; if (_sp > XB_SPIN_CAP) { atomicAdd(&(bar)[XB_TMO], 1u); break; } } } } while (0)
; __device__ __forceinline__ void lg_barrier(const XcdBarrier& b, int wave, unsigned g, unsigned nloc, bool fast) {
;     ...
;         else XB_SPIN(xb_ld(&bar[LG_GEN(g)]) == gen, bar);
;         __builtin_amdgcn_fence(__ATOMIC_ACQUIRE, "agent");
;         asm volatile("s_waitcnt vmcnt(0)" ::: "memory");
.LBB0_831:
	s_or_b64 exec, exec, s[6:7]
	s_waitcnt vmcnt(0)
	s_waitcnt vmcnt(0)

; __device__ __forceinline__ unsigned xb_ld(unsigned* p)              { return __hip_atomic_load(p, __ATOMIC_RELAXED, __HIP_MEMORY_SCOPE_AGENT); }
; __device__ __forceinline__ unsigned xb_add(unsigned* p, unsigned v) { return __hip_atomic_fetch_add(p, v, __ATOMIC_RELAXED, __HIP_MEMORY_SCOPE_AGENT); }
; #define XB_SPIN(cond, bar) do { unsigned _sp = 0; while (cond) { __builtin_amdgcn_s_sleep(1); \
;     if ((++_sp & 255u) == 0u) { if (xb_ld(&(bar)[XB_TMO])) break; if (_sp > XB_SPIN_CAP) { atomicAdd(&(bar)[XB_TMO], 1u); break; } } } } while (0)
; __device__ __forceinline__ void lg_barrier(const XcdBarrier& b, int wave, unsigned g, unsigned nloc, bool fast) {
;     ...
;         const unsigned old = xb_add(&bar[LG_SUB(g)], 1u), gen = old / nloc;
;         if (old + 1u == (gen + 1u) * nloc) xb_add(&bar[LG_GEN(g)], 1u);
;         else XB_SPIN(xb_ld(&bar[LG_GEN(g)]) == gen, bar);
;         __builtin_amdgcn_fence(__ATOMIC_ACQUIRE, "agent");
;         asm volatile("s_waitcnt vmcnt(0)" ::: "memory");
.LBB0_1025:
	s_or_b64 exec, exec, s[10:11]
	buffer_inv sc1
	s_waitcnt vmcnt(0)
	v_readfirstlane_b32 s8, v1
	s_mov_b64 s[10:11], -1
	s_nop 0
	v_add_u32_e32 v2, s8, v0
	s_add_u32 s8, s6, 0x4100
	v_and_b32_e32 v0, 31, v2
	s_addc_u32 s9, s7, 0
	v_cmp_ne_u32_e32 vcc, 31, v0
	v_mov_b64_e32 v[0:1], s[8:9]
	s_and_saveexec_b64 s[6:7], vcc
	s_cbranch_execz .LBB0_1037
	v_mov_b32_e32 v0, 0
	global_load_dword v3, v0, s[8:9] sc1
	v_lshrrev_b32_e32 v1, 5, v2
	s_mov_b64 s[14:15], 0
	s_waitcnt vmcnt(0)
	v_cmp_eq_u32_e32 vcc, v3, v1
	s_and_saveexec_b64 s[12:13], vcc
	s_cbranch_execz .LBB0_1036
	s_add_u32 s10, s80, 0x4200
	s_addc_u32 s11, s81, 0
	s_mov_b32 s26, 1
	s_branch .LBB0_1029

; __device__ __forceinline__ unsigned xb_ld(unsigned* p)              { return __hip_atomic_load(p, __ATOMIC_RELAXED, __HIP_MEMORY_SCOPE_AGENT); }
; __device__ __forceinline__ unsigned xb_add(unsigned* p, unsigned v) { return __hip_atomic_fetch_add(p, v, __ATOMIC_RELAXED, __HIP_MEMORY_SCOPE_AGENT); }
; #define XB_SPIN(cond, bar) do { unsigned _sp = 0; while (cond) { __builtin_amdgcn_s_sleep(1); \
;     if ((++_sp & 255u) == 0u) { if (xb_ld(&(bar)[XB_TMO])) break; if (_sp > XB_SPIN_CAP) { atomicAdd(&(bar)[XB_TMO], 1u); break; } } } } while (0)
; __device__ __forceinline__ void lg_barrier(const XcdBarrier& b, int wave, unsigned g, unsigned nloc, bool fast) {
;     ...
;         const unsigned old = xb_add(&bar[LG_SUB(g)], 1u), gen = old / nloc;
;         if (old + 1u == (gen + 1u) * nloc) xb_add(&bar[LG_GEN(g)], 1u);
;         else XB_SPIN(xb_ld(&bar[LG_GEN(g)]) == gen, bar);
;         __builtin_amdgcn_fence(__ATOMIC_ACQUIRE, "agent");
;         asm volatile("s_waitcnt vmcnt(0)" ::: "memory");
.LBB0_1607:
	s_or_b64 exec, exec, s[8:9]
	buffer_inv sc1
	s_waitcnt vmcnt(0)
	v_readfirstlane_b32 s6, v1
	s_mov_b64 s[8:9], -1
	s_nop 0
	v_add_u32_e32 v2, s6, v0
	s_add_u32 s6, s2, 0x4100
	v_and_b32_e32 v0, 31, v2
	s_addc_u32 s7, s3, 0
	v_cmp_ne_u32_e32 vcc, 31, v0
	v_mov_b64_e32 v[0:1], s[6:7]
	s_and_saveexec_b64 s[2:3], vcc
	s_cbranch_execz .LBB0_1619
	v_mov_b32_e32 v0, 0
	global_load_dword v3, v0, s[6:7] sc1
	v_lshrrev_b32_e32 v1, 5, v2
	s_mov_b64 s[12:13], 0
	s_waitcnt vmcnt(0)
	v_cmp_eq_u32_e32 vcc, v3, v1
	s_and_saveexec_b64 s[10:11], vcc
	s_cbranch_execz .LBB0_1618
	s_add_u32 s8, s80, 0x4200
	s_addc_u32 s9, s81, 0
	s_mov_b32 s22, 1
	s_branch .LBB0_1611

; __device__ __forceinline__ unsigned xb_ld(unsigned* p)              { return __hip_atomic_load(p, __ATOMIC_RELAXED, __HIP_MEMORY_SCOPE_AGENT); }
; #define XB_SPIN(cond, bar) do { unsigned _sp = 0; while (cond) { __builtin_amdgcn_s_sleep(1); \
;     if ((++_sp & 255u) == 0u) { if (xb_ld(&(bar)[XB_TMO])) break; if (_sp > XB_SPIN_CAP) { atomicAdd(&(bar)[XB_TMO], 1u); break; } } } } while (0)
; __device__ __forceinline__ void lg_barrier(const XcdBarrier& b, int wave, unsigned g, unsigned nloc, bool fast) {
;     ...
;         else XB_SPIN(xb_ld(&bar[LG_GEN(g)]) == gen, bar);
;         __builtin_amdgcn_fence(__ATOMIC_ACQUIRE, "agent");
;         asm volatile("s_waitcnt vmcnt(0)" ::: "memory");
.LBB0_1621:
	s_or_b64 exec, exec, s[2:3]
	s_waitcnt vmcnt(0)
	s_waitcnt vmcnt(0)

; #define WSP(type, off) ((type*)(KWS() + (off)))
;     __device__ bool next(int i, Unit& u) const {
;         const long L = (long)i * G + c; int wgid;
;         if (aligned) {
;             const int ng = (nM + WGM - 1) / WGM, gq = ng / NXCD, gr = ng % NXCD, xcd = (int)(L % NXCD); const long off = L / NXCD;
;             const int g0 = xcd * gq + (xcd < gr ? xcd : gr), g1 = g0 + gq + (xcd < gr ? 1 : 0);
;             const long w = (long)g0 * (WGM * 4) + off, wend = (long)g1 * (WGM * 4) < nwg ? (long)g1 * (WGM * 4) : nwg;
;             if (w >= wend) return false;
;             wgid = (int)w;
;         } else {
;             if (L >= nwg) return false;
;             wgid = (int)L; { const int q = nwg / NXCD, r = nwg % NXCD, xcd = wgid % NXCD, off = wgid / NXCD; wgid = (xcd < r ? xcd * (q + 1) : r * (q + 1) + (xcd - r) * q) + off; }
;         }
;         const int nig = WGM * nN, gid = wgid / nig, fm = gid * WGM, gsz = (nM - fm) < WGM ? (nM - fm) : WGM;
;         u.pm = fm + ((wgid % nig) % gsz); u.pn = (wgid % nig) / gsz;
;         int e = 0; const int r0 = u.pm * BM;
; #pragma unroll
;         for (int st = 16; st >= 1; st >>= 1) if (rb[e + st] <= r0) e += st;
;         u.pb = e * 4 + u.pn; return true;
; __global__ void __launch_bounds__(NWAVES * 64, 2) mk_fwd(Args args) {
;     ...
;         for (int rep_ = 0; rep_ < REPS(7); ++rep_) if (IN(pb0 + 2)) { bf16_t* act = WSP(bf16_t, WS_ACT); bf16_t* WDN = WSP(bf16_t, WS_WDN); bf16_t* yw = WSP(bf16_t, WS_YW); const float* lw = WSP(float, WS_LW);
;             pg8::Gemm g{act, WDN + (size_t)l * 32 * 1024 * 512, 0, 0, 512}; pg8::MoeOrder S; S.init(rb[32] / 256, G, bid, rb, LOCAL_OK()); pg8::EpiDown E{yw, lw, rb};
;             pg8::gemm_phase<pg8::EpiDown, pg8::MoeOrder, pg8::APlain, true, true>(lds, g, S, E, pg8::APlain{}, wave); }
.LBB0_1624:
	s_xor_b32 s99, s83, 0x80
	s_add_i32 s0, 0, 0x27c80
	s_mov_b64 s[10:11], s[78:79]
	s_mov_b64 s[12:13], s[78:79]
	s_mov_b64 s[2:3], s[78:79]
	s_mov_b64 s[6:7], s[78:79]
	v_mov_b32_e32 v0, s0
	ds_read_b32 v0, v0
	v_readlane_b32 s8, v251, 9
	v_readlane_b32 s9, v251, 10
	s_mov_b32 s20, s85
	s_and_b64 vcc, exec, s[8:9]
	s_waitcnt lgkmcnt(0)
	v_readfirstlane_b32 s18, v0
	s_ashr_i32 s19, s18, 31
	s_lshr_b32 s0, s19, 24
	s_add_i32 s0, s18, s0
	s_ashr_i32 s34, s0, 8
	s_lshl_b32 s0, s34, 2
	v_mbcnt_lo_u32_b32 v8, -1, 0
	v_mbcnt_hi_u32_b32 v8, -1, v8
	s_cbranch_vccz .LBB0_1628
	s_mov_b64 s[14:15], 0
	s_cmp_lt_i32 s83, s0
	s_mov_b64 s[16:17], 0
	s_cbranch_scc0 .LBB0_1629
	s_lshr_b32 s1, s19, 23
	s_add_i32 s1, s18, s1
	s_ashr_i32 s8, s1, 9
	s_lshr_b32 s1, s0, 29
	s_add_i32 s1, s0, s1
	s_and_b32 s1, s1, -8
	s_sub_i32 s9, s0, s1
	s_add_i32 s1, s8, 1
	v_readlane_b32 s17, v251, 22
	s_cmp_ge_i32 s17, s9
	s_cbranch_scc0 .LBB0_1669
	s_mul_i32 s16, s9, s1
	s_sub_i32 s9, s17, s9
	s_mul_i32 s8, s9, s8
	s_add_i32 s16, s8, s16
	s_cbranch_execz .LBB0_1670
	s_branch .LBB0_1671

;     __device__ bool next(int i, Unit& u) const {
;     ...
;             const int ng = (nM + WGM - 1) / WGM, gq = ng / NXCD, gr = ng % NXCD, xcd = (int)(L % NXCD); const long off = L / NXCD;
;             const int g0 = xcd * gq + (xcd < gr ? xcd : gr), g1 = g0 + gq + (xcd < gr ? 1 : 0);
;             const long w = (long)g0 * (WGM * 4) + off, wend = (long)g1 * (WGM * 4) < nwg ? (long)g1 * (WGM * 4) : nwg;
;             if (w >= wend) return false;
;             wgid = (int)w;
.LBB0_1630:
	s_add_i32 s8, s34, 3
	s_lshr_b32 s9, s8, 30
	s_add_i32 s9, s8, s9
	s_lshr_b32 s14, s8, 27
	s_ashr_i32 s9, s9, 2
	s_add_i32 s8, s8, s14
	s_ashr_i32 s15, s8, 5
	s_lshr_b32 s8, s9, 29
	s_add_i32 s8, s9, s8
	v_readlane_b32 s17, v251, 21
	s_xor_b32 s17, s17, 16
	s_and_b32 s8, s8, -8
	s_ashr_i32 s1, s17, 31
	s_sub_i32 s14, s9, s8
	v_readlane_b32 s21, v251, 22
	s_cmp_gt_i32 s14, s21
	s_mul_i32 s16, s15, s21
	s_cselect_b64 s[8:9], -1, 0
	s_min_i32 s14, s14, s21
	s_add_i32 s14, s14, s16
	s_cmp_lg_u64 s[8:9], 0
	s_addc_u32 s16, s14, s15
	s_ashr_i32 s15, s14, 31
	s_lshl_b64 s[8:9], s[14:15], 4
	s_add_u32 s8, s8, s17
	s_addc_u32 s9, s9, s1
	s_ashr_i32 s17, s16, 31
	s_ashr_i32 s1, s0, 31
	s_lshl_b64 s[14:15], s[16:17], 4
	v_mov_b64_e32 v[0:1], s[0:1]
	v_cmp_lt_i64_e32 vcc, s[14:15], v[0:1]
	s_and_b64 s[16:17], vcc, exec
	s_cselect_b32 s1, s15, s1
	s_cselect_b32 s14, s14, s0
	v_mov_b32_e32 v0, s14
	v_mov_b32_e32 v1, s1
	v_cmp_lt_i64_e64 s[16:17], s[8:9], v[0:1]

; template <class Epi, class Sched, class AM, bool ALIGN_EPI = false, bool SP2 = false>
; __device__ __forceinline__ void gemm_phase(PG8_LAS unsigned char* lds, const Gemm g, const Sched& S, const Epi& E, const AM& am, const int wid_in) {
;     ...
;         const bool has_next = S.next(ui + 1, nxt);
;     __device__ bool next(int i, Unit& u) const {
;         const long L = (long)i * G + c; int wgid;
;         if (aligned) {
;             const int ng = (nM + WGM - 1) / WGM, gq = ng / NXCD, gr = ng % NXCD, xcd = (int)(L % NXCD); const long off = L / NXCD;
;             const int g0 = xcd * gq + (xcd < gr ? xcd : gr), g1 = g0 + gq + (xcd < gr ? 1 : 0);
;             const long w = (long)g0 * (WGM * 4) + off, wend = (long)g1 * (WGM * 4) < nwg ? (long)g1 * (WGM * 4) : nwg;
;             if (w >= wend) return false;
;             wgid = (int)w;
;         } else {
;             if (L >= nwg) return false;
;             wgid = (int)L; { const int q = nwg / NXCD, r = nwg % NXCD, xcd = wgid % NXCD, off = wgid / NXCD; wgid = (xcd < r ? xcd * (q + 1) : r * (q + 1) + (xcd - r) * q) + off; }
.LBB0_1637:
	s_add_i32 s44, s44, 1
	s_mul_i32 s13, s44, s86
	s_mul_hi_u32 s15, s44, s33
	s_add_i32 s15, s15, s13
	s_mul_i32 s13, s44, s33
	v_readlane_b32 s16, v251, 9
	s_add_u32 s18, s13, s99
	v_readlane_b32 s17, v251, 10
	s_addc_u32 s19, s15, s89
	s_and_b64 vcc, exec, s[16:17]
	s_cbranch_vccz .LBB0_1644
	v_mov_b64_e32 v[0:1], s[0:1]
	v_cmp_lt_i64_e32 vcc, s[18:19], v[0:1]
	s_mov_b64 s[20:21], 0
	s_mov_b64 s[30:31], 0
	s_cbranch_vccz .LBB0_1645
	s_ashr_i32 s13, s18, 31
	s_lshr_b32 s13, s13, 29
	s_add_i32 s13, s18, s13
	s_and_b32 s15, s13, -8
	s_sub_i32 s15, s18, s15
	s_cmp_ge_i32 s15, s50
	s_mov_b64 s[16:17], -1
	s_cbranch_scc0 .LBB0_1641
	s_sub_i32 s16, s15, s50
	s_mul_i32 s16, s16, s49
	s_add_i32 s30, s16, s52
	s_mov_b64 s[16:17], 0

; __device__ __forceinline__ unsigned xb_ld(unsigned* p)              { return __hip_atomic_load(p, __ATOMIC_RELAXED, __HIP_MEMORY_SCOPE_AGENT); }
; __device__ __forceinline__ unsigned xb_add(unsigned* p, unsigned v) { return __hip_atomic_fetch_add(p, v, __ATOMIC_RELAXED, __HIP_MEMORY_SCOPE_AGENT); }
; #define XB_SPIN(cond, bar) do { unsigned _sp = 0; while (cond) { __builtin_amdgcn_s_sleep(1); \
;     if ((++_sp & 255u) == 0u) { if (xb_ld(&(bar)[XB_TMO])) break; if (_sp > XB_SPIN_CAP) { atomicAdd(&(bar)[XB_TMO], 1u); break; } } } } while (0)
; __device__ __forceinline__ void lg_barrier(const XcdBarrier& b, int wave, unsigned g, unsigned nloc, bool fast) {
;     ...
;         const unsigned old = xb_add(&bar[LG_SUB(g)], 1u), gen = old / nloc;
;         if (old + 1u == (gen + 1u) * nloc) xb_add(&bar[LG_GEN(g)], 1u);
;         else XB_SPIN(xb_ld(&bar[LG_GEN(g)]) == gen, bar);
;         __builtin_amdgcn_fence(__ATOMIC_ACQUIRE, "agent");
;         asm volatile("s_waitcnt vmcnt(0)" ::: "memory");
.LBB0_1795:
	s_or_b64 exec, exec, s[6:7]
	buffer_inv sc1
	s_waitcnt vmcnt(0)
	v_readfirstlane_b32 s4, v1
	s_mov_b64 s[6:7], -1
	s_nop 0
	v_add_u32_e32 v2, s4, v0
	s_add_u32 s4, s2, 0x4100
	v_and_b32_e32 v0, 31, v2
	s_addc_u32 s5, s3, 0
	v_cmp_ne_u32_e32 vcc, 31, v0
	v_mov_b64_e32 v[0:1], s[4:5]
	s_and_saveexec_b64 s[2:3], vcc
	s_cbranch_execz .LBB0_1807
	v_mov_b32_e32 v0, 0
	global_load_dword v3, v0, s[4:5] sc1
	v_lshrrev_b32_e32 v1, 5, v2
	s_mov_b64 s[10:11], 0
	s_waitcnt vmcnt(0)
	v_cmp_eq_u32_e32 vcc, v3, v1
	s_and_saveexec_b64 s[8:9], vcc
	s_cbranch_execz .LBB0_1806
	v_readlane_b32 s6, v251, 23
	v_readlane_b32 s7, v251, 24
	s_add_u32 s6, s6, 0x4200
	s_addc_u32 s7, s7, 0
	s_mov_b32 s20, 1
	s_branch .LBB0_1799

; #define WSP(type, off) ((type*)(KWS() + (off)))
;     __device__ bool next(int i, Unit& u) const {
;         const long L = (long)i * G + c; int wgid;
;         if (aligned) {
;             const int ng = (nM + WGM - 1) / WGM, gq = ng / NXCD, gr = ng % NXCD, xcd = (int)(L % NXCD); const long off = L / NXCD;
;             const int g0 = xcd * gq + (xcd < gr ? xcd : gr), g1 = g0 + gq + (xcd < gr ? 1 : 0);
;             const long w = (long)g0 * (WGM * 4) + off, wend = (long)g1 * (WGM * 4) < nwg ? (long)g1 * (WGM * 4) : nwg;
;             if (w >= wend) return false;
;             wgid = (int)w;
;         } else {
;             if (L >= nwg) return false;
;             wgid = (int)L; { const int q = nwg / NXCD, r = nwg % NXCD, xcd = wgid % NXCD, off = wgid / NXCD; wgid = (xcd < r ? xcd * (q + 1) : r * (q + 1) + (xcd - r) * q) + off; }
;         }
;         const int nig = WGM * nN, gid = wgid / nig, fm = gid * WGM, gsz = (nM - fm) < WGM ? (nM - fm) : WGM;
;         u.pm = fm + ((wgid % nig) % gsz); u.pn = (wgid % nig) / gsz;
;         int e = 0; const int r0 = u.pm * BM;
; #pragma unroll
;         for (int st = 16; st >= 1; st >>= 1) if (rb[e + st] <= r0) e += st;
;         u.pb = e * 4 + u.pn; return true;
; __global__ void __launch_bounds__(NWAVES * 64, 2) mk_fwd(Args args) {
;     ...
;         for (int rep_ = 0; rep_ < REPS(7); ++rep_) if (IN(pb0 + 2)) { bf16_t* act = WSP(bf16_t, WS_ACT); bf16_t* WDN = WSP(bf16_t, WS_WDN); bf16_t* yw = WSP(bf16_t, WS_YW); const float* lw = WSP(float, WS_LW);
;             pg8::Gemm g{act, WDN + (size_t)l * 32 * 1024 * 512, 0, 0, 512}; pg8::MoeOrder S; S.init(rb[32] / 256, G, bid, rb, LOCAL_OK()); pg8::EpiDown E{yw, lw, rb};
;             pg8::gemm_phase<pg8::EpiDown, pg8::MoeOrder, pg8::APlain, true, true>(lds, g, S, E, pg8::APlain{}, wave); }
.LBB0_2698:
	s_xor_b32 s99, s83, 0x80
	v_readlane_b32 s4, v251, 25
	v_readlane_b32 s5, v251, 26
	s_add_i32 s0, 0, 0x27c80
	s_mov_b64 s[8:9], s[4:5]
	s_mov_b64 s[10:11], s[4:5]
	s_mov_b64 s[2:3], s[4:5]
	v_mov_b32_e32 v0, s0
	ds_read_b32 v0, v0
	v_readlane_b32 s6, v251, 9
	v_readlane_b32 s7, v251, 10
	s_and_b64 vcc, exec, s[6:7]
	s_waitcnt lgkmcnt(0)
	v_readfirstlane_b32 s16, v0
	s_ashr_i32 s17, s16, 31
	s_lshr_b32 s0, s17, 24
	s_add_i32 s0, s16, s0
	s_ashr_i32 s30, s0, 8
	s_lshl_b32 s0, s30, 2
	v_mbcnt_lo_u32_b32 v8, -1, 0
	v_mbcnt_hi_u32_b32 v8, -1, v8
	s_cbranch_vccz .LBB0_2702
	s_mov_b64 s[12:13], 0
	s_cmp_lt_i32 s83, s0
	s_mov_b64 s[14:15], 0
	s_cbranch_scc0 .LBB0_2703
	s_lshr_b32 s1, s17, 23
	s_add_i32 s1, s16, s1
	s_ashr_i32 s6, s1, 9
	s_lshr_b32 s1, s0, 29
	s_add_i32 s1, s0, s1
	s_and_b32 s1, s1, -8
	s_sub_i32 s7, s0, s1
	s_add_i32 s1, s6, 1
	s_cmp_ge_i32 s62, s7
	s_cbranch_scc0 .LBB0_2743
	s_mul_i32 s14, s7, s1
	s_sub_i32 s7, s62, s7
	s_mul_i32 s6, s7, s6
	s_add_i32 s14, s6, s14
	s_cbranch_execz .LBB0_2744
	s_branch .LBB0_2745

;     __device__ bool next(int i, Unit& u) const {
;     ...
;             const int ng = (nM + WGM - 1) / WGM, gq = ng / NXCD, gr = ng % NXCD, xcd = (int)(L % NXCD); const long off = L / NXCD;
;             const int g0 = xcd * gq + (xcd < gr ? xcd : gr), g1 = g0 + gq + (xcd < gr ? 1 : 0);
;             const long w = (long)g0 * (WGM * 4) + off, wend = (long)g1 * (WGM * 4) < nwg ? (long)g1 * (WGM * 4) : nwg;
;             if (w >= wend) return false;
;             wgid = (int)w;
.LBB0_2704:
	s_add_i32 s6, s30, 3
	s_lshr_b32 s7, s6, 30
	s_add_i32 s7, s6, s7
	s_lshr_b32 s12, s6, 27
	s_ashr_i32 s7, s7, 2
	s_add_i32 s6, s6, s12
	s_ashr_i32 s13, s6, 5
	s_lshr_b32 s6, s7, 29
	s_add_i32 s6, s7, s6
	v_readlane_b32 s15, v251, 21
	s_xor_b32 s15, s15, 16
	s_and_b32 s6, s6, -8
	s_ashr_i32 s1, s15, 31
	s_sub_i32 s12, s7, s6
	s_cmp_gt_i32 s12, s62
	s_mul_i32 s14, s13, s62
	s_cselect_b64 s[6:7], -1, 0
	s_min_i32 s12, s12, s62
	s_add_i32 s12, s12, s14
	s_cmp_lg_u64 s[6:7], 0
	s_addc_u32 s14, s12, s13
	s_ashr_i32 s13, s12, 31
	s_lshl_b64 s[6:7], s[12:13], 4
	s_add_u32 s6, s6, s15
	s_addc_u32 s7, s7, s1
	s_ashr_i32 s15, s14, 31
	s_ashr_i32 s1, s0, 31
	s_lshl_b64 s[12:13], s[14:15], 4
	v_mov_b64_e32 v[0:1], s[0:1]
	v_cmp_lt_i64_e32 vcc, s[12:13], v[0:1]
	s_and_b64 s[14:15], vcc, exec
	s_cselect_b32 s1, s13, s1
	s_cselect_b32 s12, s12, s0
	v_mov_b32_e32 v0, s12
	v_mov_b32_e32 v1, s1
	v_cmp_lt_i64_e64 s[14:15], s[6:7], v[0:1]

; template <class Epi, class Sched, class AM, bool ALIGN_EPI = false, bool SP2 = false>
; __device__ __forceinline__ void gemm_phase(PG8_LAS unsigned char* lds, const Gemm g, const Sched& S, const Epi& E, const AM& am, const int wid_in) {
;     ...
;         const bool has_next = S.next(ui + 1, nxt);
;     __device__ bool next(int i, Unit& u) const {
;         const long L = (long)i * G + c; int wgid;
;         if (aligned) {
;             const int ng = (nM + WGM - 1) / WGM, gq = ng / NXCD, gr = ng % NXCD, xcd = (int)(L % NXCD); const long off = L / NXCD;
;             const int g0 = xcd * gq + (xcd < gr ? xcd : gr), g1 = g0 + gq + (xcd < gr ? 1 : 0);
;             const long w = (long)g0 * (WGM * 4) + off, wend = (long)g1 * (WGM * 4) < nwg ? (long)g1 * (WGM * 4) : nwg;
;             if (w >= wend) return false;
;             wgid = (int)w;
;         } else {
;             if (L >= nwg) return false;
;             wgid = (int)L; { const int q = nwg / NXCD, r = nwg % NXCD, xcd = wgid % NXCD, off = wgid / NXCD; wgid = (xcd < r ? xcd * (q + 1) : r * (q + 1) + (xcd - r) * q) + off; }
.LBB0_2711:
	s_add_i32 s42, s42, 1
	s_mul_i32 s11, s42, s76
	s_mul_hi_u32 s13, s42, s33
	s_add_i32 s13, s13, s11
	s_mul_i32 s11, s42, s33
	v_readlane_b32 s14, v251, 9
	s_add_u32 s16, s11, s99
	v_readlane_b32 s15, v251, 10
	s_addc_u32 s17, s13, s89
	s_and_b64 vcc, exec, s[14:15]
	s_cbranch_vccz .LBB0_2718
	v_mov_b64_e32 v[0:1], s[0:1]
	v_cmp_lt_i64_e32 vcc, s[16:17], v[0:1]
	s_mov_b64 s[18:19], 0
	s_mov_b64 s[28:29], 0
	s_cbranch_vccz .LBB0_2719
	s_ashr_i32 s11, s16, 31
	s_lshr_b32 s11, s11, 29
	s_add_i32 s11, s16, s11
	s_and_b32 s13, s11, -8
	s_sub_i32 s13, s16, s13
	s_cmp_ge_i32 s13, s48
	s_mov_b64 s[14:15], -1
	s_cbranch_scc0 .LBB0_2715
	s_sub_i32 s14, s13, s48
	s_mul_i32 s14, s14, s47
	s_add_i32 s28, s14, s50
	s_mov_b64 s[14:15], 0

; #define LAS __attribute__((address_space(3)))
; __global__ void __launch_bounds__(NWAVES * 64, 2) mk_fwd(Args args) {
;     extern __shared__ __attribute__((aligned(16))) unsigned char lds_raw[];
;     LAS unsigned char* lds = (LAS unsigned char*)lds_raw;
;     volatile LAS unsigned* MISC = (volatile LAS unsigned*)(lds + MISC_OFF);
;     LAS int* rb = (LAS int*)(lds + MISC_OFF);
;     const int wave = __builtin_amdgcn_readfirstlane((int)threadIdx.x >> 6);
	.amdhsa_kernel _Z6mk_fwd4Args
		.amdhsa_group_segment_fixed_size 0
		.amdhsa_private_segment_fixed_size 0
		.amdhsa_kernarg_size 432
		.amdhsa_user_sgpr_count 2
		.amdhsa_user_sgpr_dispatch_ptr 0
		.amdhsa_user_sgpr_queue_ptr 0
		.amdhsa_user_sgpr_kernarg_segment_ptr 1
		.amdhsa_user_sgpr_dispatch_id 0
		.amdhsa_user_sgpr_kernarg_preload_length 0
		.amdhsa_user_sgpr_kernarg_preload_offset 0
		.amdhsa_user_sgpr_private_segment_size 0
		.amdhsa_uses_dynamic_stack 0
		.amdhsa_enable_private_segment 0
		.amdhsa_system_sgpr_workgroup_id_x 1
		.amdhsa_system_sgpr_workgroup_id_y 0
		.amdhsa_system_sgpr_workgroup_id_z 0
		.amdhsa_system_sgpr_workgroup_info 0
		.amdhsa_system_vgpr_workitem_id 0
		.amdhsa_next_free_vgpr 252
		.amdhsa_next_free_sgpr 102
		.amdhsa_accum_offset 252
		.amdhsa_reserve_vcc 1
		.amdhsa_float_round_mode_32 0
		.amdhsa_float_round_mode_16_64 0
		.amdhsa_float_denorm_mode_32 3
		.amdhsa_float_denorm_mode_16_64 3
		.amdhsa_dx10_clamp 1
		.amdhsa_ieee_mode 1
		.amdhsa_fp16_overflow 0
		.amdhsa_tg_split 0
		.amdhsa_exception_fp_ieee_invalid_op 0
		.amdhsa_exception_fp_denorm_src 0
		.amdhsa_exception_fp_ieee_div_zero 0
		.amdhsa_exception_fp_ieee_overflow 0
		.amdhsa_exception_fp_ieee_underflow 0
		.amdhsa_exception_fp_ieee_inexact 0
		.amdhsa_exception_int_div_zero 0
	.end_amdhsa_kernel

; #define LAS __attribute__((address_space(3)))
; __global__ void __launch_bounds__(NWAVES * 64, 2) mk_fwd(Args args) {
;     extern __shared__ __attribute__((aligned(16))) unsigned char lds_raw[];
;     LAS unsigned char* lds = (LAS unsigned char*)lds_raw;
;     volatile LAS unsigned* MISC = (volatile LAS unsigned*)(lds + MISC_OFF);
;     LAS int* rb = (LAS int*)(lds + MISC_OFF);
;     const int wave = __builtin_amdgcn_readfirstlane((int)threadIdx.x >> 6);
amdhsa.kernels:
  - .agpr_count:     0
    .args:
      - .offset:         0
        .size:           176
        .value_kind:     by_value
      - .offset:         176
        .size:           4
        .value_kind:     hidden_block_count_x
      - .offset:         180
        .size:           4
        .value_kind:     hidden_block_count_y
      - .offset:         184
        .size:           4
        .value_kind:     hidden_block_count_z
      - .offset:         188
        .size:           2
        .value_kind:     hidden_group_size_x
      - .offset:         190
        .size:           2
        .value_kind:     hidden_group_size_y
      - .offset:         192
        .size:           2
        .value_kind:     hidden_group_size_z
      - .offset:         194
        .size:           2
        .value_kind:     hidden_remainder_x
      - .offset:         196
        .size:           2
        .value_kind:     hidden_remainder_y
      - .offset:         198
        .size:           2
        .value_kind:     hidden_remainder_z
      - .offset:         216
        .size:           8
        .value_kind:     hidden_global_offset_x
      - .offset:         224
        .size:           8
        .value_kind:     hidden_global_offset_y
      - .offset:         232
        .size:           8
        .value_kind:     hidden_global_offset_z
      - .offset:         240
        .size:           2
        .value_kind:     hidden_grid_dims
      - .offset:         296
        .size:           4
        .value_kind:     hidden_dynamic_lds_size
    .group_segment_fixed_size: 0
    .kernarg_segment_align: 8
    .kernarg_segment_size: 432
    .language:       OpenCL C
    .language_version:
      - 2
      - 0
    .max_flat_workgroup_size: 512
    .name:           _Z6mk_fwd4Args
    .private_segment_fixed_size: 0
    .sgpr_count:     108
    .sgpr_spill_count: 357
    .symbol:         _Z6mk_fwd4Args.kd
    .uniform_work_group_size: 1
    .uses_dynamic_stack: false
    .vgpr_count:     252
    .vgpr_spill_count: 0
    .wavefront_size: 64
